# v74 plus in-proj GEMM: first K-loop iteration peeled with C=0 on each accumulator's first MFMA instead of 128 v_mov zeroing per tile
# speedup vs baseline: 1.0017x; 1.0017x over previous
.LBB0_320:
	v_mov_b64_e32 v[2:3], 0x700
	s_add_u32 s14, s29, s53
	v_cmp_lt_i64_e32 vcc, s[6:7], v[2:3]
	s_addc_u32 s15, s36, 0
	s_and_b64 s[6:7], vcc, exec
	v_readlane_b32 s6, v251, 6
	s_cselect_b32 s9, s15, s3
	s_cselect_b32 s21, s14, s2
	v_readlane_b32 s7, v251, 7
	s_add_u32 s26, s6, s52
	s_addc_u32 s27, s7, 0
	s_and_b64 s[6:7], vcc, exec
	s_cselect_b32 s22, s27, s5
	s_cselect_b32 s42, s26, s4
	s_add_u32 s2, s2, 0x40080
	s_addc_u32 s3, s3, 0
	s_add_u32 s55, s4, 0x100
	s_addc_u32 s56, s5, 0
	s_mov_b32 s57, -2
	s_add_u32 s4, s2, 0xfffc0080
	s_addc_u32 s5, s3, -1
	s_add_i32 s58, 0, 0x10000
	v_add_u32_e32 v126, s58, v169
	ds_read_b128 v[82:85], v126
	ds_read_b128 v[94:97], v126 offset:1024
	ds_read_b128 v[122:125], v126 offset:2048
	ds_read_b128 v[126:129], v126 offset:3072
	s_cmp_eq_u32 s57, 12
	s_cselect_b32 s7, s9, s5
	s_cselect_b32 s6, s21, s4
	s_cselect_b32 s5, s22, s56
	s_cselect_b32 s4, s42, s55
	v_lshl_add_u64 v[184:185], s[2:3], 0, v[160:161]
	s_add_i32 m0, s37, 0xc000
	ds_read_b128 v[138:141], v171
	ds_read_b128 v[146:149], v171 offset:1024
	ds_read_b128 v[164:167], v171 offset:2048
	ds_read_b128 v[172:175], v171 offset:3072
	ds_read_b128 v[176:179], v171 offset:4096
	ds_read_b128 v[180:183], v171 offset:5120
	ds_read_b128 v[196:199], v171 offset:6144
	ds_read_b128 v[200:203], v171 offset:7168
	global_load_lds_dwordx4 v[184:185], off
	v_lshl_add_u64 v[184:185], s[2:3], 0, v[162:163]
	s_add_i32 m0, s37, 0xe000
	s_nop 0
	global_load_lds_dwordx4 v[184:185], off
	s_waitcnt lgkmcnt(8)
	s_barrier
	s_waitcnt lgkmcnt(0)
	s_setprio 1
	s_waitcnt lgkmcnt(0)
	v_mfma_f32_16x16x32_bf16 v[150:153], v[82:85], v[138:141], 0
	v_mfma_f32_16x16x32_bf16 v[142:145], v[122:125], v[138:141], 0
	v_mfma_f32_16x16x32_bf16 v[118:121], v[82:85], v[164:167], 0
	v_mfma_f32_16x16x32_bf16 v[114:117], v[122:125], v[164:167], 0
	v_mfma_f32_16x16x32_bf16 v[102:105], v[82:85], v[176:179], 0
	v_mfma_f32_16x16x32_bf16 v[98:101], v[122:125], v[176:179], 0
	v_mfma_f32_16x16x32_bf16 v[78:81], v[82:85], v[196:199], 0
	v_mfma_f32_16x16x32_bf16 v[74:77], v[122:125], v[196:199], 0
	v_mfma_f32_16x16x32_bf16 v[150:153], v[94:97], v[146:149], v[150:153]
	v_mfma_f32_16x16x32_bf16 v[142:145], v[126:129], v[146:149], v[142:145]
	v_mfma_f32_16x16x32_bf16 v[118:121], v[94:97], v[172:175], v[118:121]
	v_mfma_f32_16x16x32_bf16 v[114:117], v[126:129], v[172:175], v[114:117]
	v_mfma_f32_16x16x32_bf16 v[102:105], v[94:97], v[180:183], v[102:105]
	v_mfma_f32_16x16x32_bf16 v[98:101], v[126:129], v[180:183], v[98:101]
	v_mfma_f32_16x16x32_bf16 v[78:81], v[94:97], v[200:203], v[78:81]
	v_mfma_f32_16x16x32_bf16 v[74:77], v[126:129], v[200:203], v[74:77]
	s_setprio 0
	s_barrier
	s_add_i32 s60, 0, 0x14000
	v_add_u32_e32 v184, s60, v169
	s_add_i32 s58, s58, s28
	ds_read_b128 v[204:207], v184
	ds_read_b128 v[208:211], v184 offset:1024
	ds_read_b128 v[212:215], v184 offset:2048
	ds_read_b128 v[216:219], v184 offset:3072
	v_lshl_add_u64 v[184:185], s[4:5], 0, v[0:1]
	s_mov_b32 m0, s58
	v_lshl_add_u64 v[220:221], s[4:5], 0, v[158:159]
	global_load_lds_dwordx4 v[184:185], off
	s_add_i32 m0, s58, 0x2000
	s_nop 0
	global_load_lds_dwordx4 v[220:221], off
	s_barrier
	s_waitcnt lgkmcnt(0)
	s_setprio 1
	s_waitcnt lgkmcnt(0)
	v_mfma_f32_16x16x32_bf16 v[134:137], v[204:207], v[138:141], 0
	v_mfma_f32_16x16x32_bf16 v[130:133], v[212:215], v[138:141], 0
	v_mfma_f32_16x16x32_bf16 v[110:113], v[204:207], v[164:167], 0
	v_mfma_f32_16x16x32_bf16 v[106:109], v[212:215], v[164:167], 0
	v_mfma_f32_16x16x32_bf16 v[90:93], v[204:207], v[176:179], 0
	v_mfma_f32_16x16x32_bf16 v[86:89], v[212:215], v[176:179], 0
	v_mfma_f32_16x16x32_bf16 v[70:73], v[204:207], v[196:199], 0
	v_mfma_f32_16x16x32_bf16 v[66:69], v[212:215], v[196:199], 0
	v_mfma_f32_16x16x32_bf16 v[134:137], v[208:211], v[146:149], v[134:137]
	v_mfma_f32_16x16x32_bf16 v[130:133], v[216:219], v[146:149], v[130:133]
	v_mfma_f32_16x16x32_bf16 v[110:113], v[208:211], v[172:175], v[110:113]
	v_mfma_f32_16x16x32_bf16 v[106:109], v[216:219], v[172:175], v[106:109]
	v_mfma_f32_16x16x32_bf16 v[90:93], v[208:211], v[180:183], v[90:93]
	v_mfma_f32_16x16x32_bf16 v[86:89], v[216:219], v[180:183], v[86:89]
	v_mfma_f32_16x16x32_bf16 v[70:73], v[208:211], v[200:203], v[70:73]
	v_mfma_f32_16x16x32_bf16 v[66:69], v[216:219], v[200:203], v[66:69]
	s_setprio 0
	s_mov_b32 m0, s37
	v_lshl_add_u64 v[222:223], s[6:7], 0, v[154:155]
	s_barrier
	ds_read_b128 v[138:141], v171 offset:16384
	ds_read_b128 v[146:149], v171 offset:17408
	ds_read_b128 v[164:167], v171 offset:18432
	ds_read_b128 v[172:175], v171 offset:19456
	ds_read_b128 v[176:179], v171 offset:20480
	ds_read_b128 v[180:183], v171 offset:21504
	ds_read_b128 v[196:199], v171 offset:22528
	ds_read_b128 v[200:203], v171 offset:23552
	global_load_lds_dwordx4 v[222:223], off
	v_lshl_add_u64 v[224:225], s[6:7], 0, v[156:157]
	s_mov_b32 m0, s38
	s_nop 0
	global_load_lds_dwordx4 v[224:225], off
	s_barrier
	s_waitcnt lgkmcnt(0)
	s_setprio 1
	s_waitcnt lgkmcnt(0)
	v_mfma_f32_16x16x32_bf16 v[62:65], v[82:85], v[138:141], 0
	v_mfma_f32_16x16x32_bf16 v[58:61], v[122:125], v[138:141], 0
	v_mfma_f32_16x16x32_bf16 v[46:49], v[82:85], v[164:167], 0
	v_mfma_f32_16x16x32_bf16 v[42:45], v[122:125], v[164:167], 0
	v_mfma_f32_16x16x32_bf16 v[30:33], v[82:85], v[176:179], 0
	v_mfma_f32_16x16x32_bf16 v[26:29], v[122:125], v[176:179], 0
	v_mfma_f32_16x16x32_bf16 v[14:17], v[82:85], v[196:199], 0
	v_mfma_f32_16x16x32_bf16 v[10:13], v[122:125], v[196:199], 0
	v_mfma_f32_16x16x32_bf16 v[62:65], v[94:97], v[146:149], v[62:65]
	v_mfma_f32_16x16x32_bf16 v[58:61], v[126:129], v[146:149], v[58:61]
	v_mfma_f32_16x16x32_bf16 v[46:49], v[94:97], v[172:175], v[46:49]
	v_mfma_f32_16x16x32_bf16 v[42:45], v[126:129], v[172:175], v[42:45]
	v_mfma_f32_16x16x32_bf16 v[30:33], v[94:97], v[180:183], v[30:33]
	v_mfma_f32_16x16x32_bf16 v[26:29], v[126:129], v[180:183], v[26:29]
	v_mfma_f32_16x16x32_bf16 v[14:17], v[94:97], v[200:203], v[14:17]
	v_mfma_f32_16x16x32_bf16 v[10:13], v[126:129], v[200:203], v[10:13]
	s_setprio 0
	s_barrier
	s_add_u32 s58, s4, 0x40000
	s_addc_u32 s59, s5, 0
	s_add_i32 s60, s60, s28
	v_lshl_add_u64 v[82:83], s[58:59], 0, v[0:1]
	s_mov_b32 m0, s60
	s_nop 0
	global_load_lds_dwordx4 v[82:83], off
	v_lshl_add_u64 v[82:83], s[58:59], 0, v[158:159]
	s_add_i32 m0, s60, 0x2000
	s_nop 0
	global_load_lds_dwordx4 v[82:83], off
	s_waitcnt vmcnt(6)
	s_barrier
	s_setprio 1
	v_mfma_f32_16x16x32_bf16 v[54:57], v[204:207], v[138:141], 0
	v_mfma_f32_16x16x32_bf16 v[50:53], v[212:215], v[138:141], 0
	v_mfma_f32_16x16x32_bf16 v[38:41], v[204:207], v[164:167], 0
	v_mfma_f32_16x16x32_bf16 v[34:37], v[212:215], v[164:167], 0
	v_mfma_f32_16x16x32_bf16 v[22:25], v[204:207], v[176:179], 0
	v_mfma_f32_16x16x32_bf16 v[18:21], v[212:215], v[176:179], 0
	v_mfma_f32_16x16x32_bf16 v[6:9], v[204:207], v[196:199], 0
	v_mfma_f32_16x16x32_bf16 v[2:5], v[212:215], v[196:199], 0
	v_mfma_f32_16x16x32_bf16 v[54:57], v[208:211], v[146:149], v[54:57]
	v_mfma_f32_16x16x32_bf16 v[50:53], v[216:219], v[146:149], v[50:53]
	v_mfma_f32_16x16x32_bf16 v[38:41], v[208:211], v[172:175], v[38:41]
	v_mfma_f32_16x16x32_bf16 v[34:37], v[216:219], v[172:175], v[34:37]
	v_mfma_f32_16x16x32_bf16 v[22:25], v[208:211], v[180:183], v[22:25]
	v_mfma_f32_16x16x32_bf16 v[18:21], v[216:219], v[180:183], v[18:21]
	v_mfma_f32_16x16x32_bf16 v[6:9], v[208:211], v[200:203], v[6:9]
	v_mfma_f32_16x16x32_bf16 v[2:5], v[216:219], v[200:203], v[2:5]
	s_setprio 0
	s_add_i32 s58, 0, 0x18000
	v_add_u32_e32 v126, s58, v169
	s_barrier
	ds_read_b128 v[82:85], v126
	ds_read_b128 v[94:97], v126 offset:1024
	ds_read_b128 v[122:125], v126 offset:2048
	ds_read_b128 v[126:129], v126 offset:3072
	s_add_u32 s6, s6, 0x40000
	s_addc_u32 s7, s7, 0
	s_mov_b32 m0, s39
	v_lshl_add_u64 v[204:205], s[6:7], 0, v[154:155]
	ds_read_b128 v[138:141], v171 offset:32768
	ds_read_b128 v[146:149], v171 offset:33792
	ds_read_b128 v[164:167], v171 offset:34816
	ds_read_b128 v[172:175], v171 offset:35840
	ds_read_b128 v[176:179], v171 offset:36864
	ds_read_b128 v[180:183], v171 offset:37888
	ds_read_b128 v[196:199], v171 offset:38912
	ds_read_b128 v[200:203], v171 offset:39936
	global_load_lds_dwordx4 v[204:205], off
	v_lshl_add_u64 v[204:205], s[6:7], 0, v[156:157]
	s_mov_b32 m0, s46
	s_nop 0
	global_load_lds_dwordx4 v[204:205], off
	s_waitcnt lgkmcnt(8)
	s_barrier
	s_waitcnt lgkmcnt(0)
	s_setprio 1
	s_waitcnt lgkmcnt(0)
	v_mfma_f32_16x16x32_bf16 v[150:153], v[82:85], v[138:141], v[150:153]
	v_mfma_f32_16x16x32_bf16 v[142:145], v[122:125], v[138:141], v[142:145]
	v_mfma_f32_16x16x32_bf16 v[118:121], v[82:85], v[164:167], v[118:121]
	v_mfma_f32_16x16x32_bf16 v[114:117], v[122:125], v[164:167], v[114:117]
	v_mfma_f32_16x16x32_bf16 v[102:105], v[82:85], v[176:179], v[102:105]
	v_mfma_f32_16x16x32_bf16 v[98:101], v[122:125], v[176:179], v[98:101]
	v_mfma_f32_16x16x32_bf16 v[78:81], v[82:85], v[196:199], v[78:81]
	v_mfma_f32_16x16x32_bf16 v[74:77], v[122:125], v[196:199], v[74:77]
	v_mfma_f32_16x16x32_bf16 v[150:153], v[94:97], v[146:149], v[150:153]
	v_mfma_f32_16x16x32_bf16 v[142:145], v[126:129], v[146:149], v[142:145]
	v_mfma_f32_16x16x32_bf16 v[118:121], v[94:97], v[172:175], v[118:121]
	v_mfma_f32_16x16x32_bf16 v[114:117], v[126:129], v[172:175], v[114:117]
	v_mfma_f32_16x16x32_bf16 v[102:105], v[94:97], v[180:183], v[102:105]
	v_mfma_f32_16x16x32_bf16 v[98:101], v[126:129], v[180:183], v[98:101]
	v_mfma_f32_16x16x32_bf16 v[78:81], v[94:97], v[200:203], v[78:81]
	v_mfma_f32_16x16x32_bf16 v[74:77], v[126:129], v[200:203], v[74:77]
	s_setprio 0
	s_barrier
	s_add_i32 s6, 0, 0x1c000
	s_add_i32 s7, s58, s28
	v_add_u32_e32 v187, s6, v169
	v_lshl_add_u64 v[184:185], v[184:185], 0, s[44:45]
	s_mov_b32 m0, s7
	ds_read_b128 v[204:207], v187
	ds_read_b128 v[208:211], v187 offset:1024
	ds_read_b128 v[212:215], v187 offset:2048
	ds_read_b128 v[216:219], v187 offset:3072
	global_load_lds_dwordx4 v[184:185], off
	v_lshl_add_u64 v[184:185], v[220:221], 0, s[44:45]
	s_add_i32 m0, s7, 0x2000
	s_nop 0
	global_load_lds_dwordx4 v[184:185], off
	s_barrier
	s_waitcnt lgkmcnt(0)
	s_setprio 1
	s_waitcnt lgkmcnt(0)
	v_mfma_f32_16x16x32_bf16 v[134:137], v[204:207], v[138:141], v[134:137]
	v_mfma_f32_16x16x32_bf16 v[130:133], v[212:215], v[138:141], v[130:133]
	v_mfma_f32_16x16x32_bf16 v[110:113], v[204:207], v[164:167], v[110:113]
	v_mfma_f32_16x16x32_bf16 v[106:109], v[212:215], v[164:167], v[106:109]
	v_mfma_f32_16x16x32_bf16 v[90:93], v[204:207], v[176:179], v[90:93]
	v_mfma_f32_16x16x32_bf16 v[86:89], v[212:215], v[176:179], v[86:89]
	v_mfma_f32_16x16x32_bf16 v[70:73], v[204:207], v[196:199], v[70:73]
	v_mfma_f32_16x16x32_bf16 v[66:69], v[212:215], v[196:199], v[66:69]
	v_mfma_f32_16x16x32_bf16 v[134:137], v[208:211], v[146:149], v[134:137]
	v_mfma_f32_16x16x32_bf16 v[130:133], v[216:219], v[146:149], v[130:133]
	v_mfma_f32_16x16x32_bf16 v[110:113], v[208:211], v[172:175], v[110:113]
	v_mfma_f32_16x16x32_bf16 v[106:109], v[216:219], v[172:175], v[106:109]
	v_mfma_f32_16x16x32_bf16 v[90:93], v[208:211], v[180:183], v[90:93]
	v_mfma_f32_16x16x32_bf16 v[86:89], v[216:219], v[180:183], v[86:89]
	v_mfma_f32_16x16x32_bf16 v[70:73], v[208:211], v[200:203], v[70:73]
	v_mfma_f32_16x16x32_bf16 v[66:69], v[216:219], v[200:203], v[66:69]
	s_setprio 0
	s_mov_b32 m0, s47
	v_lshl_add_u64 v[184:185], v[222:223], 0, s[44:45]
	s_barrier
	ds_read_b128 v[138:141], v171 offset:49152
	ds_read_b128 v[146:149], v171 offset:50176
	ds_read_b128 v[164:167], v171 offset:51200
	ds_read_b128 v[172:175], v171 offset:52224
	ds_read_b128 v[176:179], v171 offset:53248
	ds_read_b128 v[180:183], v171 offset:54272
	ds_read_b128 v[196:199], v171 offset:55296
	ds_read_b128 v[200:203], v171 offset:56320
	global_load_lds_dwordx4 v[184:185], off
	v_lshl_add_u64 v[184:185], v[224:225], 0, s[44:45]
	s_mov_b32 m0, s48
	s_nop 0
	global_load_lds_dwordx4 v[184:185], off
	s_barrier
	s_waitcnt lgkmcnt(0)
	s_setprio 1
	s_waitcnt lgkmcnt(0)
	v_mfma_f32_16x16x32_bf16 v[62:65], v[82:85], v[138:141], v[62:65]
	v_mfma_f32_16x16x32_bf16 v[58:61], v[122:125], v[138:141], v[58:61]
	v_mfma_f32_16x16x32_bf16 v[46:49], v[82:85], v[164:167], v[46:49]
	v_mfma_f32_16x16x32_bf16 v[42:45], v[122:125], v[164:167], v[42:45]
	v_mfma_f32_16x16x32_bf16 v[30:33], v[82:85], v[176:179], v[30:33]
	v_mfma_f32_16x16x32_bf16 v[26:29], v[122:125], v[176:179], v[26:29]
	v_mfma_f32_16x16x32_bf16 v[14:17], v[82:85], v[196:199], v[14:17]
	v_mfma_f32_16x16x32_bf16 v[10:13], v[122:125], v[196:199], v[10:13]
	v_mfma_f32_16x16x32_bf16 v[62:65], v[94:97], v[146:149], v[62:65]
	v_mfma_f32_16x16x32_bf16 v[58:61], v[126:129], v[146:149], v[58:61]
	v_mfma_f32_16x16x32_bf16 v[46:49], v[94:97], v[172:175], v[46:49]
	v_mfma_f32_16x16x32_bf16 v[42:45], v[126:129], v[172:175], v[42:45]
	v_mfma_f32_16x16x32_bf16 v[30:33], v[94:97], v[180:183], v[30:33]
	v_mfma_f32_16x16x32_bf16 v[26:29], v[126:129], v[180:183], v[26:29]
	v_mfma_f32_16x16x32_bf16 v[14:17], v[94:97], v[200:203], v[14:17]
	v_mfma_f32_16x16x32_bf16 v[10:13], v[126:129], v[200:203], v[10:13]
	s_setprio 0
	s_barrier
	s_add_u32 s4, s4, 0x40080
	s_addc_u32 s5, s5, 0
	s_add_i32 s6, s6, s28
	v_lshl_add_u64 v[82:83], s[4:5], 0, v[0:1]
	s_mov_b32 m0, s6
	s_nop 0
	global_load_lds_dwordx4 v[82:83], off
	v_lshl_add_u64 v[82:83], s[4:5], 0, v[158:159]
	s_add_i32 m0, s6, 0x2000
	s_nop 0
	global_load_lds_dwordx4 v[82:83], off
	s_waitcnt vmcnt(6)
	s_barrier
	s_setprio 1
	v_mfma_f32_16x16x32_bf16 v[54:57], v[204:207], v[138:141], v[54:57]
	v_mfma_f32_16x16x32_bf16 v[50:53], v[212:215], v[138:141], v[50:53]
	v_mfma_f32_16x16x32_bf16 v[38:41], v[204:207], v[164:167], v[38:41]
	v_mfma_f32_16x16x32_bf16 v[34:37], v[212:215], v[164:167], v[34:37]
	v_mfma_f32_16x16x32_bf16 v[22:25], v[204:207], v[176:179], v[22:25]
	v_mfma_f32_16x16x32_bf16 v[18:21], v[212:215], v[176:179], v[18:21]
	v_mfma_f32_16x16x32_bf16 v[6:9], v[204:207], v[196:199], v[6:9]
	v_mfma_f32_16x16x32_bf16 v[2:5], v[212:215], v[196:199], v[2:5]
	v_mfma_f32_16x16x32_bf16 v[54:57], v[208:211], v[146:149], v[54:57]
	v_mfma_f32_16x16x32_bf16 v[50:53], v[216:219], v[146:149], v[50:53]
	v_mfma_f32_16x16x32_bf16 v[38:41], v[208:211], v[172:175], v[38:41]
	v_mfma_f32_16x16x32_bf16 v[34:37], v[216:219], v[172:175], v[34:37]
	v_mfma_f32_16x16x32_bf16 v[22:25], v[208:211], v[180:183], v[22:25]
	v_mfma_f32_16x16x32_bf16 v[18:21], v[216:219], v[180:183], v[18:21]
	v_mfma_f32_16x16x32_bf16 v[6:9], v[208:211], v[200:203], v[6:9]
	v_mfma_f32_16x16x32_bf16 v[2:5], v[216:219], v[200:203], v[2:5]
	s_setprio 0
	s_add_i32 s57, s57, 2
	s_add_u32 s2, s2, 0x100
	s_addc_u32 s3, s3, 0
	s_add_u32 s55, s55, 0x100
	s_addc_u32 s56, s56, 0
	s_cmp_gt_u32 s57, 13
	s_barrier
